# baseline (speedup 1.0000x reference)
.LBB1_11:
	s_or_b64 exec, exec, s[28:29]
	s_add_i32 s28, s22, 1
	s_ashr_i32 s29, s28, 31
	s_lshl_b64 s[28:29], s[28:29], 7
	s_add_u32 s50, s43, s28
	s_addc_u32 s51, s44, s29
	v_lshl_add_u64 v[0:1], s[50:51], 0, v[128:129]
	v_readfirstlane_b32 s43, v177
	v_lshl_add_u64 v[2:3], v[0:1], 0, v[134:135]
	s_mov_b32 m0, s43
	v_readfirstlane_b32 s43, v178
	s_add_u32 s44, s45, s28
	s_waitcnt vmcnt(4)
	s_barrier
	global_load_lds_dwordx4 v[2:3], off
	v_lshl_add_u64 v[0:1], v[0:1], 0, v[136:137]
	s_mov_b32 m0, s43
	s_addc_u32 s45, s46, s29
	global_load_lds_dwordx4 v[0:1], off
	v_lshl_add_u64 v[0:1], s[44:45], 0, v[128:129]
	v_readfirstlane_b32 s43, v167
	v_lshl_add_u64 v[2:3], v[0:1], 0, v[134:135]
	s_mov_b32 m0, s43
	v_readfirstlane_b32 s43, v168
	s_add_u32 s28, s47, s28
	global_load_lds_dwordx4 v[2:3], off
	v_lshl_add_u64 v[0:1], v[0:1], 0, v[136:137]
	s_mov_b32 m0, s43
	s_addc_u32 s29, s48, s29
	global_load_lds_dwordx4 v[0:1], off
	v_lshl_add_u64 v[0:1], s[28:29], 0, v[128:129]
	v_readfirstlane_b32 s28, v179
	v_add_u32_e32 v146, 0x2000, v179
	v_lshl_add_u64 v[2:3], v[0:1], 0, v[134:135]
	s_mov_b32 m0, s28
	v_readfirstlane_b32 s28, v146
	global_load_lds_dwordx4 v[2:3], off
	v_lshl_add_u64 v[0:1], v[0:1], 0, v[136:137]
	s_mov_b32 m0, s28
	v_mov_b32_e32 v127, 0
	global_load_lds_dwordx4 v[0:1], off
	s_cmp_lt_i32 s41, 3
	v_mov_b32_e32 v126, v127
	v_mov_b32_e32 v125, v127
	v_mov_b32_e32 v124, v127
	v_mov_b32_e32 v123, v127
	v_mov_b32_e32 v122, v127
	v_mov_b32_e32 v121, v127
	v_mov_b32_e32 v120, v127
	v_mov_b32_e32 v119, v127
	v_mov_b32_e32 v118, v127
	v_mov_b32_e32 v117, v127
	v_mov_b32_e32 v116, v127
	v_mov_b32_e32 v115, v127
	v_mov_b32_e32 v114, v127
	v_mov_b32_e32 v113, v127
	v_mov_b32_e32 v112, v127
	v_mov_b32_e32 v111, v127
	v_mov_b32_e32 v110, v127
	v_mov_b32_e32 v109, v127
	v_mov_b32_e32 v108, v127
	v_mov_b32_e32 v107, v127
	v_mov_b32_e32 v106, v127
	v_mov_b32_e32 v105, v127
	v_mov_b32_e32 v104, v127
	v_mov_b32_e32 v103, v127
	v_mov_b32_e32 v102, v127
	v_mov_b32_e32 v101, v127
	v_mov_b32_e32 v100, v127
	v_mov_b32_e32 v99, v127
	v_mov_b32_e32 v98, v127
	v_mov_b32_e32 v97, v127
	v_mov_b32_e32 v96, v127
	v_mov_b32_e32 v95, v127
	v_mov_b32_e32 v94, v127
	v_mov_b32_e32 v93, v127
	v_mov_b32_e32 v92, v127
	v_mov_b32_e32 v91, v127
	v_mov_b32_e32 v90, v127
	v_mov_b32_e32 v89, v127
	v_mov_b32_e32 v88, v127
	v_mov_b32_e32 v87, v127
	v_mov_b32_e32 v86, v127
	v_mov_b32_e32 v85, v127
	v_mov_b32_e32 v84, v127
	v_mov_b32_e32 v83, v127
	v_mov_b32_e32 v82, v127
	v_mov_b32_e32 v81, v127
	v_mov_b32_e32 v80, v127
	v_mov_b32_e32 v79, v127
	v_mov_b32_e32 v78, v127
	v_mov_b32_e32 v77, v127
	v_mov_b32_e32 v76, v127
	v_mov_b32_e32 v75, v127
	v_mov_b32_e32 v74, v127
	v_mov_b32_e32 v73, v127
	v_mov_b32_e32 v72, v127
	v_mov_b32_e32 v71, v127
	v_mov_b32_e32 v70, v127
	v_mov_b32_e32 v69, v127
	v_mov_b32_e32 v68, v127
	v_mov_b32_e32 v67, v127
	v_mov_b32_e32 v66, v127
	v_mov_b32_e32 v65, v127
	v_mov_b32_e32 v64, v127
	v_mov_b32_e32 v63, v127
	v_mov_b32_e32 v62, v127
	v_mov_b32_e32 v61, v127
	v_mov_b32_e32 v60, v127
	v_mov_b32_e32 v59, v127
	v_mov_b32_e32 v58, v127
	v_mov_b32_e32 v57, v127
	v_mov_b32_e32 v56, v127
	v_mov_b32_e32 v55, v127
	v_mov_b32_e32 v54, v127
	v_mov_b32_e32 v53, v127
	v_mov_b32_e32 v52, v127
	v_mov_b32_e32 v51, v127
	v_mov_b32_e32 v50, v127
	v_mov_b32_e32 v49, v127
	v_mov_b32_e32 v48, v127
	v_mov_b32_e32 v47, v127
	v_mov_b32_e32 v46, v127
	v_mov_b32_e32 v45, v127
	v_mov_b32_e32 v44, v127
	v_mov_b32_e32 v43, v127
	v_mov_b32_e32 v42, v127
	v_mov_b32_e32 v41, v127
	v_mov_b32_e32 v40, v127
	v_mov_b32_e32 v39, v127
	v_mov_b32_e32 v38, v127
	v_mov_b32_e32 v37, v127
	v_mov_b32_e32 v36, v127
	v_mov_b32_e32 v35, v127
	v_mov_b32_e32 v34, v127
	v_mov_b32_e32 v33, v127
	v_mov_b32_e32 v32, v127
	v_mov_b32_e32 v31, v127
	v_mov_b32_e32 v30, v127
	v_mov_b32_e32 v29, v127
	v_mov_b32_e32 v28, v127
	v_mov_b32_e32 v27, v127
	v_mov_b32_e32 v26, v127
	v_mov_b32_e32 v25, v127
	v_mov_b32_e32 v24, v127
	v_mov_b32_e32 v23, v127
	v_mov_b32_e32 v22, v127
	v_mov_b32_e32 v21, v127
	v_mov_b32_e32 v20, v127
	v_mov_b32_e32 v19, v127
	v_mov_b32_e32 v18, v127
	v_mov_b32_e32 v17, v127
	v_mov_b32_e32 v16, v127
	v_mov_b32_e32 v15, v127
	v_mov_b32_e32 v14, v127
	v_mov_b32_e32 v13, v127
	v_mov_b32_e32 v12, v127
	v_mov_b32_e32 v11, v127
	v_mov_b32_e32 v10, v127
	v_mov_b32_e32 v9, v127
	v_mov_b32_e32 v8, v127
	v_mov_b32_e32 v7, v127
	v_mov_b32_e32 v6, v127
	v_mov_b32_e32 v5, v127
	v_mov_b32_e32 v4, v127
	v_mov_b32_e32 v3, v127
	v_mov_b32_e32 v2, v127
	v_mov_b32_e32 v1, v127
	v_mov_b32_e32 v0, v127
	s_waitcnt vmcnt(6)
	s_barrier
	s_cbranch_scc1 .LBB1_14
	s_lshl_b64 s[28:29], s[4:5], 12
	s_lshl_b64 s[44:45], s[20:21], 12
	s_lshl_b64 s[24:25], s[24:25], 12
	s_lshl_b64 s[26:27], s[26:27], 12
	s_add_i32 s5, s41, -2
	v_lshl_add_u64 v[138:139], s[26:27], 1, v[130:131]
	v_lshl_add_u64 v[140:141], s[28:29], 1, v[132:133]
	v_lshl_add_u64 v[142:143], s[44:45], 1, v[130:131]
	v_lshl_add_u64 v[144:145], s[24:25], 1, v[132:133]
	s_mov_b32 s21, 0
	.p2align	6

.LBB2_11:
	v_and_b32_e32 v28, 8, v0
	v_lshlrev_b32_e32 v0, 1, v5
	v_lshl_or_b32 v38, v6, 4, v0
	v_lshlrev_b32_e32 v0, 7, v1
	v_mov_b32_e32 v29, 0xeeeeeeee
	v_mov_b32_e32 v30, 0x44444444
	v_cmp_eq_u32_e32 vcc, 0, v28
	v_lshl_add_u64 v[2:3], s[20:21], 0, v[2:3]
	v_lshl_or_b32 v40, s24, 9, v0
	v_cndmask_b32_e64 v0, 0, 1, s[0:1]
	v_cndmask_b32_e32 v28, v29, v30, vcc
	s_waitcnt vmcnt(9)
	v_and_b32_e32 v44, 0xffff, v8
	s_waitcnt vmcnt(8)
	v_and_b32_e32 v43, 0xffff, v9
	s_waitcnt vmcnt(7)
	v_and_b32_e32 v42, 0xffff, v11
	s_waitcnt vmcnt(3)
	v_and_b32_e32 v41, 0xffff, v24
	v_and_b32_e32 v29, 0xffff, v10
	v_and_b32_e32 v30, 0xffff, v12
	s_waitcnt vmcnt(2)
	v_and_b32_e32 v31, 0xffff, v13
	s_waitcnt vmcnt(1)
	v_and_b32_e32 v32, 0xffff, v15
	v_and_b32_e32 v45, 0xffff, v14
	s_waitcnt vmcnt(0)
	v_and_b32_e32 v33, 0xffff, v25
	s_mov_b32 s19, 0x20000
	s_mov_b32 s18, 0x40000
	s_and_b32 s17, s9, 0xffff
	s_mov_b32 s16, s8
	v_lshl_add_u64 v[24:25], v[16:17], 2, v[2:3]
	v_lshlrev_b32_e32 v35, 9, v4
	v_lshlrev_b32_e32 v36, 7, v7
	v_lshlrev_b32_e32 v37, 4, v5
	v_cmp_eq_u32_e64 s[2:3], 0, v4
	v_lshl_add_u32 v34, v1, 10, v35
	v_add3_u32 v34, v34, v36, v37
	v_add_u32_e32 v121, 1, v1
	v_add_u32_e32 v122, 2, v1
	v_add_u32_e32 v123, 3, v1
	v_and_b32_e32 v121, 3, v121
	v_and_b32_e32 v122, 3, v122
	v_and_b32_e32 v123, 3, v123
	v_lshl_add_u32 v121, v121, 10, v35
	v_lshl_add_u32 v122, v122, 10, v35
	v_lshl_add_u32 v123, v123, 10, v35
	v_add3_u32 v121, v121, v36, v37
	v_add3_u32 v122, v122, v36, v37
	v_add3_u32 v123, v123, v36, v37
	v_lshl_or_b32 v39, v27, 14, v34
	s_mov_b64 s[6:7], 0
	s_mov_b32 s28, 0x10000
	v_cmp_ne_u32_e64 s[0:1], 1, v0
	v_mov_b32_e32 v46, 0
	s_mov_b32 s29, 0
	v_lshl_add_u32 v120, v27, 14, v40
	v_or_b32_e32 v120, v120, v38
	s_mov_b32 s37, 0
	s_cmp_eq_u32 s29, 0
	s_cbranch_scc1 .LBB2_23
	.p2align	6
